# v34 + barrier clean-up: barrier 12 also waits on the TOP counter; the unused generation words are no longer bumped (two atomics + ack waits off the last leader's exit path)
# speedup vs baseline: 1.0048x; 1.0048x over previous
.LBB0_109:
	s_or_b64 exec, exec, s[8:9]
	v_cvt_f32_u32_e32 v4, v1
	s_waitcnt vmcnt(0)
	v_readfirstlane_b32 s6, v3
	s_add_u32 s8, s50, 0x7500
	s_addc_u32 s9, s51, 0
	v_rcp_iflag_f32_e32 v4, v4
	v_add_u32_e32 v2, s6, v2
	v_add_u32_e32 v5, 1, v2
	s_mov_b64 s[10:11], 0
	v_mul_f32_e32 v3, 0x4f7ffffe, v4
	v_cvt_u32_f32_e32 v3, v3
	v_sub_u32_e32 v4, 0, v1
	v_mul_lo_u32 v4, v4, v3
	v_mul_hi_u32 v4, v3, v4
	v_add_u32_e32 v3, v3, v4
	v_mul_hi_u32 v3, v2, v3
	v_mul_lo_u32 v4, v3, v1
	v_sub_u32_e32 v2, v2, v4
	v_add_u32_e32 v6, 1, v3
	v_cmp_ge_u32_e32 vcc, v2, v1
	v_sub_u32_e32 v4, v2, v1
	s_nop 0
	v_cndmask_b32_e32 v3, v3, v6, vcc
	v_cndmask_b32_e32 v2, v2, v4, vcc
	v_add_u32_e32 v4, 1, v3
	v_cmp_ge_u32_e32 vcc, v2, v1
	s_nop 1
	v_cndmask_b32_e32 v4, v3, v4, vcc
	v_mul_lo_u32 v2, v1, v4
	v_add_u32_e32 v1, v2, v1
	v_cmp_ne_u32_e32 vcc, v5, v1
	v_mov_b64_e32 v[2:3], s[8:9]
	s_and_saveexec_b64 s[6:7], vcc
	s_cbranch_execz .LBB0_121
	v_mov_b32_e32 v5, v1
	s_add_u32 s100, s50, 0x7400
	s_addc_u32 s101, s51, 0
	v_mov_b32_e32 v1, 0
	global_load_dword v2, v1, s[100:101] sc1
	s_mov_b64 s[14:15], 0
	s_waitcnt vmcnt(0)
	v_cmp_lt_u32_e32 vcc, v2, v5
	s_and_saveexec_b64 s[12:13], vcc
	s_cbranch_execz .LBB0_120
	s_add_u32 s10, s50, 0x4200
	s_addc_u32 s11, s51, 0
	s_mov_b32 s24, 1
	s_branch .LBB0_113

.LBB0_2025:
	s_or_b64 exec, exec, s[8:9]
	v_cvt_f32_u32_e32 v4, v2
	s_waitcnt vmcnt(0)
	v_readfirstlane_b32 s6, v3
	v_sub_u32_e32 v3, 0, v2
	v_rcp_iflag_f32_e32 v4, v4
	v_add_u32_e32 v5, s6, v1
	v_mul_f32_e32 v4, 0x4f7ffffe, v4
	v_cvt_u32_f32_e32 v4, v4
	v_mul_lo_u32 v1, v3, v4
	v_mul_hi_u32 v1, v4, v1
	v_add_u32_e32 v1, v4, v1
	v_mul_hi_u32 v1, v5, v1
	v_mul_lo_u32 v3, v1, v2
	v_sub_u32_e32 v3, v5, v3
	v_add_u32_e32 v4, 1, v1
	v_cmp_ge_u32_e32 vcc, v3, v2
	s_nop 1
	v_cndmask_b32_e32 v1, v1, v4, vcc
	v_sub_u32_e32 v4, v3, v2
	v_cndmask_b32_e32 v3, v3, v4, vcc
	v_add_u32_e32 v4, 1, v1
	v_cmp_ge_u32_e32 vcc, v3, v2
	v_add_u32_e32 v3, 1, v5
	s_nop 0
	v_cndmask_b32_e32 v1, v1, v4, vcc
	v_mul_lo_u32 v4, v2, v1
	v_add_u32_e32 v2, v4, v2
	v_cmp_ne_u32_e32 vcc, v3, v2
	s_and_saveexec_b64 s[6:7], vcc
	s_xor_b64 s[6:7], exec, s[6:7]
	s_cbranch_execz .LBB0_2039
	s_waitcnt lgkmcnt(0)
	v_add_u32_e32 v4, 1, v1
	v_mul_lo_u32 v4, v4, v0
	v_mov_b32_e32 v0, 0x7000
	global_load_dword v0, v0, s[50:51] offset:1024 sc1
	s_add_u32 s12, s50, 0x7400
	s_addc_u32 s13, s51, 0
	s_waitcnt vmcnt(0)
	v_cmp_lt_u32_e32 vcc, v0, v4
	s_and_saveexec_b64 s[8:9], vcc
	s_cbranch_execz .LBB0_2038
	s_add_u32 s10, s50, 0x4200
	s_addc_u32 s11, s51, 0
	s_mov_b32 s24, 1
	s_mov_b64 s[14:15], 0
	v_mov_b32_e32 v0, 0
	s_branch .LBB0_2029

.LBB0_2031:
	global_load_dword v2, v0, s[12:13] sc1
	s_add_i32 s24, s24, 1
	s_mov_b64 s[20:21], -1
	s_waitcnt vmcnt(0)
	v_cmp_ge_u32_e32 vcc, v2, v4
	s_orn2_b64 s[18:19], vcc, exec
	s_branch .LBB0_2028

.LBB0_2042:
	s_or_b64 exec, exec, s[8:9]
	v_cvt_f32_u32_e32 v3, v0
	s_waitcnt vmcnt(0)
	v_readfirstlane_b32 s6, v2
	s_add_u32 s8, s50, 0x7500
	s_addc_u32 s9, s51, 0
	v_rcp_iflag_f32_e32 v3, v3
	v_add_u32_e32 v1, s6, v1
	v_add_u32_e32 v4, 1, v1
	s_mov_b64 s[10:11], 0
	v_mul_f32_e32 v2, 0x4f7ffffe, v3
	v_cvt_u32_f32_e32 v2, v2
	v_sub_u32_e32 v3, 0, v0
	v_mul_lo_u32 v3, v3, v2
	v_mul_hi_u32 v3, v2, v3
	v_add_u32_e32 v2, v2, v3
	v_mul_hi_u32 v2, v1, v2
	v_mul_lo_u32 v3, v2, v0
	v_sub_u32_e32 v1, v1, v3
	v_add_u32_e32 v5, 1, v2
	v_cmp_ge_u32_e32 vcc, v1, v0
	v_sub_u32_e32 v3, v1, v0
	s_nop 0
	v_cndmask_b32_e32 v2, v2, v5, vcc
	v_cndmask_b32_e32 v1, v1, v3, vcc
	v_add_u32_e32 v3, 1, v2
	v_cmp_ge_u32_e32 vcc, v1, v0
	s_nop 1
	v_cndmask_b32_e32 v2, v2, v3, vcc
	v_mul_lo_u32 v1, v0, v2
	v_add_u32_e32 v0, v1, v0
	v_cmp_ne_u32_e32 vcc, v4, v0
	v_mov_b32_e32 v4, v0
	v_mov_b64_e32 v[0:1], s[8:9]
	s_and_saveexec_b64 s[6:7], vcc
	s_cbranch_execz .LBB0_2054
	s_add_u32 s100, s50, 0x7400
	s_addc_u32 s101, s51, 0
	v_mov_b32_e32 v0, 0
	global_load_dword v1, v0, s[100:101] sc1
	s_mov_b64 s[14:15], 0
	s_waitcnt vmcnt(0)
	v_cmp_lt_u32_e32 vcc, v1, v4
	s_and_saveexec_b64 s[12:13], vcc
	s_cbranch_execz .LBB0_2053
	s_add_u32 s10, s50, 0x4200
	s_addc_u32 s11, s51, 0
	s_mov_b32 s24, 1
	s_branch .LBB0_2046

.LBB0_2048:
	global_load_dword v1, v0, s[100:101] sc1
	s_add_i32 s24, s24, 1
	s_mov_b64 s[18:19], -1
	s_waitcnt vmcnt(0)
	v_cmp_ge_u32_e32 vcc, v1, v4
	s_orn2_b64 s[22:23], vcc, exec
	s_branch .LBB0_2045
